# speedup vs baseline: 1.0005x; 1.0005x over previous
_Z11proj_kernelPKfS0_S0_PKDF16_S0_S0_S0_PDF16_S3_S3_Pj:
	s_and_b32 s3, s2, 7
	s_lshr_b32 s2, s2, 3
	s_mul_i32 s3, s3, 24
	s_add_i32 s2, s2, s3
	s_ashr_i32 s12, s2, 6
	s_load_dwordx8 s[4:11], s[0:1], 0x0
	s_cmp_gt_u32 s2, 63
	s_cselect_b64 s[22:23], -1, 0
	s_cmp_lg_u32 s12, 1
	s_cselect_b64 s[18:19], -1, 0
	s_cmp_eq_u32 s12, 1
	s_cselect_b64 s[20:21], -1, 0
	s_and_b64 s[14:15], s[20:21], exec
	s_waitcnt lgkmcnt(0)
	s_cselect_b32 s14, s6, s8
	s_cselect_b32 s15, s7, s9
	s_ashr_i32 s13, s12, 31
	s_lshl_b32 s28, s2, 7
	s_lshl_b64 s[6:7], s[12:13], 19
	s_and_b32 s3, s28, 0x1f80
	s_cmp_lt_u32 s2, 64
	s_cselect_b64 vcc, -1, 0
	v_lshrrev_b32_e32 v1, 2, v0
	v_lshrrev_b32_e32 v2, 2, v0
	v_and_b32_e32 v2, 0x70, v2
	v_bfe_u32 v254, v0, 3, 3
	v_or_b32_e32 v254, v2, v254
	v_or_b32_e32 v2, s3, v254
	s_and_b64 s[8:9], vcc, exec
	s_cselect_b32 s25, s5, s15
	s_cselect_b32 s24, s4, s14
	v_lshlrev_b32_e32 v2, 11, v2
	v_mov_b32_e32 v3, 0
	v_lshlrev_b32_e32 v6, 4, v0
	s_add_u32 s4, s10, s6
	v_lshl_add_u64 v[4:5], s[24:25], 0, v[2:3]
	v_and_b32_e32 v6, 0x70, v6
	v_mov_b32_e32 v7, v3
	v_lshlrev_b32_e32 v56, 4, v0
	v_mov_b32_e32 v57, v3
	s_addc_u32 s5, s11, s7
	v_lshl_add_u64 v[4:5], v[4:5], 0, v[6:7]
	s_mov_b64 s[46:47], 0x4000
	v_lshl_add_u64 v[250:251], v[4:5], 0, s[46:47]
	s_movk_i32 s8, 0x2000
	v_lshl_add_u64 v[6:7], s[4:5], 0, v[56:57]
	global_load_dwordx4 v[8:11], v[4:5], off sc1 nt
	global_load_dwordx4 v[12:15], v[250:251], off sc1 nt
	global_load_dwordx4 v[16:19], v56, s[4:5] sc1
	v_add_co_u32_e64 v28, s[4:5], s8, v6
	s_mov_b32 s33, 0xa000
	s_nop 0
	v_addc_co_u32_e64 v29, s[4:5], 0, v7, s[4:5]
	s_movk_i32 s4, 0x4000
	s_nop 0
	v_add_co_u32_e64 v30, s[4:5], s4, v6
	s_mov_b32 s6, 0xe000
	s_nop 0
	v_addc_co_u32_e64 v31, s[4:5], 0, v7, s[4:5]
	global_load_dwordx4 v[20:23], v[28:29], off sc1
	global_load_dwordx4 v[24:27], v[30:31], off sc1
	s_movk_i32 s4, 0x6000
	v_add_co_u32_e64 v40, s[4:5], s4, v6
	v_lshlrev_b32_e32 v57, 6, v1
	s_nop 0
	v_addc_co_u32_e64 v41, s[4:5], 0, v7, s[4:5]
	global_load_dwordx4 v[28:31], v[40:41], off sc1
	global_load_dwordx4 v[32:35], v[4:5], off offset:128 sc1 nt
	global_load_dwordx4 v[36:39], v[250:251], off offset:128 sc1 nt
	s_mov_b32 s4, 0x8000
	v_add_co_u32_e64 v40, s[4:5], s4, v6
	v_bitop3_b32 v58, v56, 48, v0 bitop3:0x48
	s_nop 0
	v_addc_co_u32_e64 v41, s[4:5], 0, v7, s[4:5]
	v_add_co_u32_e64 v44, s[4:5], s33, v6
	global_load_dwordx4 v[40:43], v[40:41], off sc1
	s_nop 0
	v_addc_co_u32_e64 v45, s[4:5], 0, v7, s[4:5]
	s_mov_b32 s4, 0xc000
	s_nop 0
	v_add_co_u32_e64 v48, s[4:5], s4, v6
	global_load_dwordx4 v[44:47], v[44:45], off sc1
	s_nop 0
	v_addc_co_u32_e64 v49, s[4:5], 0, v7, s[4:5]
	v_add_co_u32_e64 v52, s[4:5], s6, v6
	global_load_dwordx4 v[48:51], v[48:49], off sc1
	s_nop 0
	v_addc_co_u32_e64 v53, s[4:5], 0, v7, s[4:5]
	global_load_dwordx4 v[52:55], v[52:53], off sc1
	s_mov_b32 s4, 0x1e000
	v_bfe_u32 v57, v0, 1, 2
	v_bfe_u32 v58, v254, 2, 2
	v_xor_b32_e32 v57, v57, v58
	v_lshlrev_b32_e32 v57, 4, v57
	v_and_b32_e32 v58, 1, v0
	v_lshl_or_b32 v57, v58, 3, v57
	v_lshl_add_u32 v209, v254, 6, v57
	v_xor_b32_e32 v248, 32, v209
	v_add_u32_e32 v248, 0x200, v248
	v_add_u32_e32 v208, 0, v56
	v_readfirstlane_b32 s30, v0
	v_bfe_u32 v207, v0, 5, 1
	v_bitop3_b32 v1, v207, v1, 3 bitop3:0x78
	v_lshlrev_b32_e32 v210, 4, v1
	s_mov_b32 s34, 0x14000
	v_add_u32_e32 v213, 0x2000, v208
	s_mov_b32 s43, 0
	s_lshr_b32 s29, s30, 6
	s_mov_b32 s35, -2
	s_mov_b32 s36, 0xffff2000
	s_mov_b32 s37, 0xffff4000
	s_mov_b32 s38, 0xffff6000
	s_movk_i32 s39, 0x8000
	s_movk_i32 s40, 0xa000
	s_movk_i32 s41, 0xc000
	s_movk_i32 s42, 0xe000
	s_mov_b64 s[26:27], 0x100
	v_mov_b32_e32 v56, v3
	v_mov_b32_e32 v57, v3
	v_mov_b32_e32 v58, v3
	v_mov_b32_e32 v59, v3
	v_mov_b32_e32 v60, v3
	v_mov_b32_e32 v61, v3
	v_mov_b32_e32 v62, v3
	v_mov_b32_e32 v63, v3
	v_mov_b32_e32 v64, v3
	v_mov_b32_e32 v65, v3
	v_mov_b32_e32 v66, v3
	v_mov_b32_e32 v67, v3
	v_mov_b32_e32 v68, v3
	v_mov_b32_e32 v69, v3
	v_mov_b32_e32 v70, v3
	s_waitcnt vmcnt(11)
	v_cvt_pk_f16_f32 v8, v8, v9
	v_cvt_pk_f16_f32 v9, v10, v11
	s_waitcnt vmcnt(10)
	v_cvt_pk_f16_f32 v10, v12, v13
	v_cvt_pk_f16_f32 v11, v14, v15
	ds_write_b64 v209, v[8:9]
	ds_write_b64 v248, v[10:11]
	v_and_b32_e32 v10, 31, v0
	s_waitcnt vmcnt(9)
	ds_write_b128 v208, v[16:19] offset:8192
	s_waitcnt vmcnt(8)
	ds_write_b128 v208, v[20:23] offset:16384
	s_waitcnt vmcnt(7)
	ds_write_b128 v208, v[24:27] offset:24576
	s_load_dwordx2 s[16:17], s[0:1], 0x50
	s_load_dwordx4 s[12:15], s[0:1], 0x40
	s_load_dwordx8 s[4:11], s[0:1], 0x20
	s_lshl_b32 s0, s30, 1
	s_and_b32 s31, s0, 0x180
	s_lshr_b32 s0, s30, 2
	v_bfe_u32 v11, v0, 2, 2
	s_and_b32 s0, s0, 0x3fffffc0
	s_waitcnt vmcnt(5)
	v_cvt_pk_f16_f32 v8, v32, v33
	v_cvt_pk_f16_f32 v9, v34, v35
	v_or_b32_e32 v12, s31, v10
	v_or_b32_e32 v206, s0, v10
	v_bitop3_b32 v1, v207, v11, 2 bitop3:0x36
	s_waitcnt vmcnt(4)
	v_cvt_pk_f16_f32 v10, v36, v37
	v_cvt_pk_f16_f32 v11, v38, v39
	s_mov_b32 s0, 0x10000
	ds_write_b128 v208, v[28:31] offset:32768
	ds_write_b64 v209, v[8:9] offset:40960
	ds_write_b64 v248, v[10:11] offset:40960
	v_add_co_u32_e64 v8, s[0:1], s0, v6
	global_load_dwordx4 v[154:157], v[250:251], off offset:256 sc1 nt
	global_load_dwordx4 v[162:165], v[4:5], off offset:256 sc1 nt
	v_addc_co_u32_e64 v9, s[0:1], 0, v7, s[0:1]
	s_mov_b32 s0, 0x12000
	global_load_dwordx4 v[158:161], v[8:9], off sc1
	v_add_co_u32_e64 v8, s[0:1], s0, v6
	v_lshl_add_u32 v211, v12, 6, 0
	s_nop 0
	v_addc_co_u32_e64 v9, s[0:1], 0, v7, s[0:1]
	v_add_co_u32_e64 v10, s[0:1], s34, v6
	v_add_u32_e32 v14, 0x12000, v208
	s_nop 0
	v_addc_co_u32_e64 v11, s[0:1], 0, v7, s[0:1]
	s_mov_b32 s0, 0x16000
	s_nop 0
	v_add_co_u32_e64 v12, s[0:1], s0, v6
	s_waitcnt vmcnt(3)
	ds_write_b128 v14, v[52:55]
	v_addc_co_u32_e64 v13, s[0:1], 0, v7, s[0:1]
	s_mov_b32 s0, 0x18000
	s_nop 0
	v_add_co_u32_e64 v14, s[0:1], s0, v6
	ds_write_b128 v208, v[40:43] offset:49152
	s_nop 0
	v_addc_co_u32_e64 v15, s[0:1], 0, v7, s[0:1]
	s_mov_b32 s0, 0x1a000
	s_nop 0
	v_add_co_u32_e64 v16, s[0:1], s0, v6
	ds_write_b128 v208, v[44:47] offset:57344
	s_nop 0
	v_addc_co_u32_e64 v17, s[0:1], 0, v7, s[0:1]
	s_mov_b32 s0, 0x1c000
	ds_write_b128 v213, v[48:51] offset:57344
	v_add_co_u32_e64 v18, s[0:1], s0, v6
	v_add_u32_e32 v216, v211, v210
	s_nop 0
	v_addc_co_u32_e64 v19, s[0:1], 0, v7, s[0:1]
	global_load_dwordx4 v[174:177], v[8:9], off sc1
	global_load_dwordx4 v[166:169], v[10:11], off sc1
	global_load_dwordx4 v[170:173], v[12:13], off sc1
	global_load_dwordx4 v[142:145], v[250:251], off offset:384 sc1 nt
	global_load_dwordx4 v[150:153], v[4:5], off offset:384 sc1 nt
	global_load_dwordx4 v[138:141], v[14:15], off sc1
	global_load_dwordx4 v[146:149], v[16:17], off sc1
	global_load_dwordx4 v[134:137], v[18:19], off sc1
	s_mov_b32 s0, 0x1e000
	v_add_co_u32_e64 v8, s[0:1], s0, v6
	s_nop 1
	v_addc_co_u32_e64 v9, s[0:1], 0, v7, s[0:1]
	global_load_dwordx4 v[130:133], v[8:9], off sc1
	s_waitcnt lgkmcnt(0)
	s_barrier
	v_lshl_add_u32 v218, v206, 6, 0
	v_add_u32_e32 v217, v218, v210
	ds_read_b128 v[198:201], v216 offset:8192
	ds_read_b128 v[194:197], v216 offset:10240
	ds_read_b128 v[190:193], v216 offset:12288
	ds_read_b128 v[178:181], v216 offset:14336
	ds_read_b128 v[186:189], v217
	ds_read_b128 v[182:185], v217 offset:2048
	v_and_b32_e32 v20, 7, v0
	v_lshl_or_b32 v2, v20, 4, v2
	s_mov_b64 s[0:1], 0x2e000
	v_lshlrev_b32_e32 v212, 4, v1
	v_lshl_add_u64 v[202:203], v[6:7], 0, s[0:1]
	s_mov_b64 s[0:1], 0x290
	v_lshl_add_u64 v[4:5], s[24:25], 0, v[2:3]
	v_lshl_add_u64 v[204:205], v[4:5], 0, s[0:1]
	v_lshl_add_u64 v[252:253], v[204:205], 0, s[46:47]
	s_mov_b64 s[24:25], 0x10000
	v_mov_b32_e32 v2, v3
	v_mov_b32_e32 v4, v3
	v_mov_b32_e32 v5, v3
	v_mov_b32_e32 v6, v3
	v_mov_b32_e32 v7, v3
	v_mov_b32_e32 v8, v3
	v_mov_b32_e32 v9, v3
	v_mov_b32_e32 v10, v3
	v_mov_b32_e32 v11, v3
	v_mov_b32_e32 v12, v3
	v_mov_b32_e32 v13, v3
	v_mov_b32_e32 v14, v3
	v_mov_b32_e32 v15, v3
	v_mov_b32_e32 v16, v3
	v_mov_b32_e32 v17, v3
	v_mov_b32_e32 v18, v3
	v_mov_b32_e32 v19, v3
	v_mov_b32_e32 v20, v3
	v_mov_b32_e32 v21, v3
	v_mov_b32_e32 v22, v3
	v_mov_b32_e32 v23, v3
	v_mov_b32_e32 v24, v3
	v_mov_b32_e32 v25, v3
	v_mov_b32_e32 v26, v3
	v_mov_b32_e32 v27, v3
	v_mov_b32_e32 v28, v3
	v_mov_b32_e32 v29, v3
	v_mov_b32_e32 v30, v3
	v_mov_b32_e32 v31, v3
	v_mov_b32_e32 v32, v3
	v_mov_b32_e32 v33, v3
	v_mov_b32_e32 v34, v3
	v_mov_b32_e32 v35, v3
	v_mov_b32_e32 v36, v3
	v_mov_b32_e32 v37, v3
	v_mov_b32_e32 v38, v3
	v_mov_b32_e32 v39, v3
	v_mov_b32_e32 v40, v3
	v_mov_b32_e32 v41, v3
	v_mov_b32_e32 v42, v3
	v_mov_b32_e32 v43, v3
	v_mov_b32_e32 v44, v3
	v_mov_b32_e32 v45, v3
	v_mov_b32_e32 v46, v3
	v_mov_b32_e32 v47, v3
	v_mov_b32_e32 v48, v3
	v_mov_b32_e32 v49, v3
	v_mov_b32_e32 v50, v3
	v_mov_b32_e32 v51, v3
	v_mov_b32_e32 v52, v3
	v_mov_b32_e32 v53, v3
	v_mov_b32_e32 v54, v3
	v_mov_b32_e32 v55, v3
	v_mov_b32_e32 v71, v3
	v_mov_b32_e32 v72, v3
	v_mov_b32_e32 v73, v3
	v_mov_b32_e32 v74, v3
	v_mov_b32_e32 v75, v3
	v_mov_b32_e32 v76, v3
	v_mov_b32_e32 v77, v3
	v_mov_b32_e32 v78, v3
	v_mov_b32_e32 v79, v3
	v_mov_b32_e32 v80, v3
	v_mov_b32_e32 v81, v3
	v_mov_b32_e32 v82, v3
	v_mov_b32_e32 v83, v3
	v_mov_b32_e32 v84, v3
	v_mov_b32_e32 v85, v3
	v_mov_b32_e32 v86, v3
	v_mov_b32_e32 v87, v3
	v_mov_b32_e32 v88, v3
	v_mov_b32_e32 v89, v3
	v_mov_b32_e32 v90, v3
	v_mov_b32_e32 v91, v3
	v_mov_b32_e32 v92, v3
	v_mov_b32_e32 v93, v3
	v_mov_b32_e32 v94, v3
	v_mov_b32_e32 v95, v3
	v_mov_b32_e32 v96, v3
	v_mov_b32_e32 v97, v3
	v_mov_b32_e32 v98, v3
	v_mov_b32_e32 v99, v3
	v_mov_b32_e32 v100, v3
	v_mov_b32_e32 v101, v3
	v_mov_b32_e32 v102, v3
	v_mov_b32_e32 v103, v3
	v_mov_b32_e32 v104, v3
	v_mov_b32_e32 v105, v3
	v_mov_b32_e32 v106, v3
	v_mov_b32_e32 v107, v3
	v_mov_b32_e32 v108, v3
	v_mov_b32_e32 v109, v3
	v_mov_b32_e32 v110, v3
	v_mov_b32_e32 v111, v3
	v_mov_b32_e32 v112, v3
	v_mov_b32_e32 v113, v3
	v_mov_b32_e32 v114, v3
	v_mov_b32_e32 v115, v3
	v_mov_b32_e32 v116, v3
	v_mov_b32_e32 v117, v3
	v_mov_b32_e32 v118, v3
	v_mov_b32_e32 v119, v3
	v_mov_b32_e32 v120, v3
	v_mov_b32_e32 v121, v3
	v_mov_b32_e32 v122, v3
	v_mov_b32_e32 v123, v3
	v_mov_b32_e32 v124, v3
	v_mov_b32_e32 v125, v3
	v_mov_b32_e32 v126, v3
	v_mov_b32_e32 v127, v3
	v_mov_b32_e32 v128, v3
	v_mov_b32_e32 v129, v3
	v_and_b32_e32 v1, 63, v0
	v_add_u32_e32 v215, v211, v212
	v_add_u32_e32 v214, v218, v212
